# baseline (speedup 1.0000x reference)
.LBB1_2:
	s_or_b64 exec, exec, s[2:3]
	v_and_b32_e32 v52, 3, v52
	v_and_b32_e32 v54, 48, v0
	v_lshlrev_b32_e32 v55, 2, v0
	v_lshl_or_b32 v54, v50, 6, v54
	v_and_b32_e32 v55, 32, v55
	v_lshlrev_b32_e32 v56, 14, v53
	v_lshlrev_b32_e32 v57, 13, v52
	v_lshl_or_b32 v52, v52, 6, s20
	v_lshlrev_b32_e32 v51, 2, v51
	s_movk_i32 s2, 0x4c
	v_bitop3_b32 v191, v54, v57, v55 bitop3:0xde
	v_bitop3_b32 v192, v54, v56, v55 bitop3:0xde
	v_or_b32_e32 v54, v52, v51
	v_bitop3_b32 v51, v52, s2, v51 bitop3:0xc8
	v_lshrrev_b32_e32 v52, 6, v52
	s_lshl_b32 s2, s19, 2
	v_and_or_b32 v52, v52, 14, s18
	v_lshlrev_b32_e32 v182, 2, v51
	v_mov_b32_e32 v183, 0
	s_add_u32 s2, s8, s2
	v_lshlrev_b32_e32 v52, 14, v52
	v_lshlrev_b32_e32 v53, 7, v53
	v_lshl_add_u64 v[184:185], s[10:11], 0, v[182:183]
	s_addc_u32 s3, s9, 0
	v_lshlrev_b32_e32 v182, 2, v54
	v_or3_b32 v193, v53, v52, v50
	s_mov_b32 s18, 0
	v_lshl_add_u64 v[186:187], s[2:3], 0, v[182:183]
	s_mov_b32 s2, s6
	s_mov_b32 s3, s7
	s_movk_i32 s8, 0x2000
	s_movk_i32 s9, 0x6000
	s_mov_b32 s10, 0xa000
	s_mov_b32 s11, 0xe000
	s_mov_b32 s19, 0
	s_mov_b32 s20, 0
	v_readfirstlane_b32 s26, v0
	s_nop 3
	s_lshr_b32 s26, s26, 8
	s_cmp_eq_u32 s26, 0
	s_cbranch_scc1 .Lnoprio
	s_setprio 1
.Lnoprio:
	s_branch .Lfirst
